# tconv8 prologue: first B-operand loads issued before the last prologue barrier instead of after it
# baseline (speedup 1.0000x reference)
.LBB0_538:
	s_or_b64 exec, exec, s[4:5]
	v_add_u32_e32 v0, -7, v17
	v_ldexp_f32 v184, 1.0, v0
	s_waitcnt lgkmcnt(0)
	v_alignbyte_b32 v14, v11, v10, 1
	v_alignbyte_b32 v15, v6, v11, 1
	v_alignbyte_b32 v31, v7, v6, 1
	v_mov_b32_e32 v4, v10
	v_mov_b32_e32 v5, v11
	v_add_u32_e32 v0, 0x10890, v193
	v_alignbyte_b32 v12, v9, v8, 1
	v_alignbyte_b32 v13, v10, v9, 1
	v_alignbyte_b32 v16, v9, v8, 2
	v_alignbyte_b32 v17, v10, v9, 2
	v_alignbyte_b32 v18, v11, v10, 2
	v_alignbyte_b32 v19, v6, v11, 2
	v_alignbyte_b32 v20, v9, v8, 3
	v_alignbyte_b32 v21, v10, v9, 3
	v_alignbyte_b32 v22, v11, v10, 3
	v_alignbyte_b32 v23, v6, v11, 3
	v_pk_mov_b32 v[24:25], v[8:9], v[10:11] op_sel:[1,0]
	v_pk_mov_b32 v[26:27], v[10:11], v[6:7] op_sel:[1,0]
	v_alignbyte_b32 v35, v7, v6, 2
	ds_write_b128 v0, v[4:7]
	v_alignbyte_b32 v11, v2, v7, 1
	v_mov_b32_e32 v8, v14
	v_mov_b32_e32 v9, v15
	v_mov_b32_e32 v10, v31
	v_add_u32_e32 v0, 0x129b0, v193
	v_alignbyte_b32 v39, v7, v6, 3
	ds_write_b128 v0, v[8:11]
	v_alignbyte_b32 v45, v2, v7, 2
	v_mov_b32_e32 v42, v18
	v_mov_b32_e32 v43, v19
	v_mov_b32_e32 v44, v35
	v_add_u32_e32 v0, 0x14ad0, v193
	ds_write_b128 v0, v[42:45]
	v_alignbyte_b32 v49, v2, v7, 3
	v_mov_b32_e32 v46, v22
	v_mov_b32_e32 v47, v23
	v_mov_b32_e32 v48, v39
	v_add_u32_e32 v0, 0x16bf0, v193
	ds_write_b128 v0, v[46:49]
	v_pk_mov_b32 v[6:7], v[6:7], v[2:3] op_sel:[1,0]
	v_mov_b32_e32 v4, v26
	v_mov_b32_e32 v5, v27
	v_add_u32_e32 v0, 0x18c80, v193
	ds_write_b128 v0, v[4:7]
	v_alignbyte_b32 v7, v3, v2, 1
	v_mov_b32_e32 v4, v15
	v_mov_b32_e32 v5, v31
	v_mov_b32_e32 v6, v11
	v_add_u32_e32 v0, 0x1ada0, v193
	ds_write_b128 v0, v[4:7]
	v_alignbyte_b32 v7, v3, v2, 2
	v_mov_b32_e32 v4, v19
	v_mov_b32_e32 v5, v35
	v_mov_b32_e32 v6, v45
	v_add_u32_e32 v0, 0x1cec0, v193
	ds_write_b128 v0, v[4:7]
	v_alignbyte_b32 v3, v3, v2, 3
	v_mov_b32_e32 v0, v23
	v_mov_b32_e32 v1, v39
	v_mov_b32_e32 v2, v49
	v_add_u32_e32 v4, 0x1efe0, v193
	ds_write_b128 v4, v[0:3]
	v_lshl_add_u64 v[0:1], s[36:37], 0, v[178:179]
	v_lshlrev_b64 v[186:187], 12, v[0:1]
	v_mov_b32_e32 v28, v13
	v_mov_b32_e32 v29, v14
	v_mov_b32_e32 v30, v15
	v_mov_b32_e32 v32, v17
	v_mov_b32_e32 v33, v18
	v_mov_b32_e32 v34, v19
	v_mov_b32_e32 v36, v21
	v_mov_b32_e32 v37, v22
	v_mov_b32_e32 v38, v23
	v_lshl_add_u64 v[188:189], v[180:181], 0, v[186:187]
	global_load_dwordx4 v[0:3], v[188:189], off
	global_load_dwordx4 v[4:7], v[188:189], off offset:16
	ds_write_b128 v193, v[12:15] offset:8480
	ds_write_b128 v193, v[16:19] offset:16960
	ds_write_b128 v193, v[20:23] offset:25440
	ds_write_b128 v193, v[24:27] offset:33808
	ds_write_b128 v193, v[28:31] offset:42288
	ds_write_b128 v193, v[32:35] offset:50768
	ds_write_b128 v193, v[36:39] offset:59248
	s_waitcnt lgkmcnt(0)
	s_barrier
	ds_read_b128 v[8:11], v192 offset:416
	ds_read_b128 v[12:15], v192 offset:432
	ds_read_b128 v[16:19], v192 offset:448
	ds_read_b128 v[20:23], v192 offset:464
	ds_read_b128 v[24:27], v192 offset:480
	ds_read_b128 v[28:31], v192 offset:496
	ds_read_b128 v[32:35], v192 offset:512
	s_mov_b32 s4, 0
	v_mov_b32_e32 v41, v40
	v_mov_b32_e32 v42, v40
	v_mov_b32_e32 v43, v40
	v_mov_b32_e32 v44, v40
	v_mov_b32_e32 v45, v40
	v_mov_b32_e32 v46, v40
	v_mov_b32_e32 v47, v40
	v_mov_b32_e32 v48, v40
	v_mov_b32_e32 v49, v40
	v_mov_b32_e32 v50, v40
	v_mov_b32_e32 v51, v40
	v_mov_b32_e32 v52, v40
	v_mov_b32_e32 v53, v40
	v_mov_b32_e32 v54, v40
	v_mov_b32_e32 v55, v40
	v_mov_b32_e32 v56, v40
	v_mov_b32_e32 v57, v40
	v_mov_b32_e32 v58, v40
	v_mov_b32_e32 v59, v40
	v_mov_b32_e32 v60, v40
	v_mov_b32_e32 v61, v40
	v_mov_b32_e32 v62, v40
	v_mov_b32_e32 v63, v40
	v_mov_b32_e32 v64, v40
	v_mov_b32_e32 v65, v40
	v_mov_b32_e32 v66, v40
	v_mov_b32_e32 v67, v40
	v_mov_b32_e32 v68, v40
	v_mov_b32_e32 v69, v40
	v_mov_b32_e32 v70, v40
	v_mov_b32_e32 v71, v40
	v_mov_b32_e32 v72, v40
	v_mov_b32_e32 v73, v40
	v_mov_b32_e32 v74, v40
	v_mov_b32_e32 v75, v40
	v_mov_b32_e32 v76, v40
	v_mov_b32_e32 v77, v40
	v_mov_b32_e32 v78, v40
	v_mov_b32_e32 v79, v40
	v_mov_b32_e32 v80, v40
	v_mov_b32_e32 v81, v40
	v_mov_b32_e32 v82, v40
	v_mov_b32_e32 v83, v40
	v_mov_b32_e32 v84, v40
	v_mov_b32_e32 v85, v40
	v_mov_b32_e32 v86, v40
	v_mov_b32_e32 v87, v40
	v_mov_b32_e32 v88, v40
	v_mov_b32_e32 v89, v40
	v_mov_b32_e32 v90, v40
	v_mov_b32_e32 v91, v40
	v_mov_b32_e32 v92, v40
	v_mov_b32_e32 v93, v40
	v_mov_b32_e32 v94, v40
	v_mov_b32_e32 v95, v40
	v_mov_b32_e32 v96, v40
	v_mov_b32_e32 v97, v40
	v_mov_b32_e32 v98, v40
	v_mov_b32_e32 v99, v40
	v_mov_b32_e32 v100, v40
	v_mov_b32_e32 v101, v40
	v_mov_b32_e32 v102, v40
	v_mov_b32_e32 v103, v40
	v_mov_b32_e32 v104, v40
	v_mov_b32_e32 v105, v40
	v_mov_b32_e32 v106, v40
	v_mov_b32_e32 v107, v40
	v_mov_b32_e32 v108, v40
	v_mov_b32_e32 v109, v40
	v_mov_b32_e32 v110, v40
	v_mov_b32_e32 v111, v40
	v_mov_b32_e32 v112, v40
	v_mov_b32_e32 v113, v40
	v_mov_b32_e32 v114, v40
	v_mov_b32_e32 v115, v40
	v_mov_b32_e32 v116, v40
	v_mov_b32_e32 v117, v40
	v_mov_b32_e32 v118, v40
	v_mov_b32_e32 v119, v40
	v_mov_b32_e32 v120, v40
	v_mov_b32_e32 v121, v40
	v_mov_b32_e32 v122, v40
	v_mov_b32_e32 v123, v40
	v_mov_b32_e32 v124, v40
	v_mov_b32_e32 v125, v40
	v_mov_b32_e32 v126, v40
	v_mov_b32_e32 v127, v40
	v_mov_b32_e32 v128, v40
	v_mov_b32_e32 v129, v40
	v_mov_b32_e32 v130, v40
	v_mov_b32_e32 v131, v40
	v_mov_b32_e32 v132, v40
	v_mov_b32_e32 v133, v40
	v_mov_b32_e32 v134, v40
	v_mov_b32_e32 v135, v40
	v_mov_b32_e32 v136, v40
	v_mov_b32_e32 v137, v40
	v_mov_b32_e32 v138, v40
	v_mov_b32_e32 v139, v40
	v_mov_b32_e32 v140, v40
	v_mov_b32_e32 v141, v40
	v_mov_b32_e32 v142, v40
	v_mov_b32_e32 v143, v40
	v_mov_b32_e32 v144, v40
	v_mov_b32_e32 v145, v40
	v_mov_b32_e32 v146, v40
	v_mov_b32_e32 v147, v40
	v_mov_b32_e32 v148, v40
	v_mov_b32_e32 v149, v40
	v_mov_b32_e32 v150, v40
	v_mov_b32_e32 v151, v40
	v_mov_b32_e32 v152, v40
	v_mov_b32_e32 v153, v40
	v_mov_b32_e32 v154, v40
	v_mov_b32_e32 v155, v40
	v_mov_b32_e32 v156, v40
	v_mov_b32_e32 v157, v40
	v_mov_b32_e32 v158, v40
	v_mov_b32_e32 v159, v40
	v_mov_b32_e32 v160, v40
	v_mov_b32_e32 v161, v40
	v_mov_b32_e32 v162, v40
	v_mov_b32_e32 v163, v40
	v_mov_b32_e32 v164, v40
	v_mov_b32_e32 v165, v40
	v_mov_b32_e32 v166, v40
	v_mov_b32_e32 v167, v40
